# all PEER table conversion deferred into the idle workgroups of layer-0 gemm2/3/4 last rounds
# baseline (speedup 1.0000x reference)
.LBB0_34:
	s_andn2_b64 vcc, exec, s[22:23]
	s_cbranch_vccnz .LBB0_38
.LBB0_38:
	s_mov_b64 s[22:23], 0

.LBB0_611:
	v_readlane_b32 s4, v255, 36
	v_readlane_b32 s8, v252, 0
	s_add_i32 s5, s4, 7
	v_readlane_b32 s9, v252, 1
	s_cmp_ge_i32 s5, s9
	v_readlane_b32 s10, v252, 2
	v_readlane_b32 s11, v252, 3
	s_cbranch_scc1 .LBB0_661
	v_readlane_b32 s4, v255, 34
	s_nop 0
	s_cmp_lg_u32 s4, 0
	s_cbranch_scc1 .Ldfu_done
	s_cmp_gt_u32 s82, 32
	s_cselect_b32 s11, 32, 0
	s_cmp_lt_u32 s2, s11
	s_cbranch_scc1 .Ldfu_done
	s_sub_u32 s10, s82, s11
	s_lshl_b32 s10, s10, 3
	s_sub_u32 s4, s2, s11
	s_lshl_b32 s4, s4, 3
	v_readfirstlane_b32 s11, v0
	s_lshr_b32 s11, s11, 6
	s_add_u32 s4, s4, s11
	s_add_u32 s4, s4, 0x0
	s_cmp_ge_u32 s4, 0x8000
	s_cbranch_scc1 .Ldfu_done
	v_readlane_b32 s6, v252, 4
	v_readlane_b32 s7, v252, 5
	s_nop 0
	s_sub_u32 s6, s6, 0x38
	s_subb_u32 s7, s7, 0
	s_load_dwordx2 s[8:9], s[6:7], 0x0
	s_load_dwordx2 s[6:7], s[6:7], 0x20
	v_and_b32_e32 v6, 63, v0
	v_lshlrev_b32_e32 v7, 4, v6
	v_lshrrev_b32_e32 v56, 5, v6
	v_and_b32_e32 v57, 31, v6
	v_lshlrev_b32_e32 v56, 21, v56
	v_lshl_add_u32 v56, v57, 2, v56
	v_add_u32_e32 v56, 0xaa00000, v56
	s_mov_b64 exec, -1
	s_waitcnt lgkmcnt(0)
	s_lshl_b32 s11, s4, 13
	v_add_u32_e32 v40, s11, v7
	v_add_u32_e32 v41, 0x1000, v40
	global_load_dwordx4 v[8:11], v40, s[8:9] nt
	global_load_dwordx4 v[12:15], v40, s[8:9] offset:1024 nt
	global_load_dwordx4 v[16:19], v40, s[8:9] offset:2048 nt
	global_load_dwordx4 v[20:23], v40, s[8:9] offset:3072 nt
	global_load_dwordx4 v[24:27], v41, s[8:9] nt
	global_load_dwordx4 v[28:31], v41, s[8:9] offset:1024 nt
	global_load_dwordx4 v[32:35], v41, s[8:9] offset:2048 nt
	global_load_dwordx4 v[36:39], v41, s[8:9] offset:3072 nt
.Ldfu_loop:
	s_add_u32 s11, s4, s10
	s_min_u32 s11, s11, 0x7fff
	s_mov_b32 s101, s11
	s_lshl_b32 s11, s101, 13
	v_add_u32_e32 v40, s11, v7
	v_add_u32_e32 v41, 0x1000, v40
	global_load_dwordx4 v[76:79], v40, s[8:9] nt
	global_load_dwordx4 v[80:83], v40, s[8:9] offset:1024 nt
	global_load_dwordx4 v[84:87], v40, s[8:9] offset:2048 nt
	global_load_dwordx4 v[88:91], v40, s[8:9] offset:3072 nt
	global_load_dwordx4 v[92:95], v41, s[8:9] nt
	global_load_dwordx4 v[96:99], v41, s[8:9] offset:1024 nt
	global_load_dwordx4 v[100:103], v41, s[8:9] offset:2048 nt
	global_load_dwordx4 v[104:107], v41, s[8:9] offset:3072 nt
	s_waitcnt vmcnt(8)
	v_max3_f32 v42, |v8|, |v9|, |v10|
	v_max3_f32 v43, |v12|, |v13|, |v14|
	v_max3_f32 v44, |v16|, |v17|, |v18|
	v_max3_f32 v45, |v20|, |v21|, |v22|
	v_max3_f32 v46, |v24|, |v25|, |v26|
	v_max3_f32 v47, |v28|, |v29|, |v30|
	v_max3_f32 v48, |v32|, |v33|, |v34|
	v_max3_f32 v49, |v36|, |v37|, |v38|
	v_max_f32_e64 v42, v42, |v11|
	v_max_f32_e64 v43, v43, |v15|
	v_max_f32_e64 v44, v44, |v19|
	v_max_f32_e64 v45, v45, |v23|
	v_max_f32_e64 v46, v46, |v27|
	v_max_f32_e64 v47, v47, |v31|
	v_max_f32_e64 v48, v48, |v35|
	v_max_f32_e64 v49, v49, |v39|
	v_max3_f32 v42, v42, v43, v44
	v_max3_f32 v45, v45, v46, v47
	v_max3_f32 v42, v42, v45, v48
	v_max_f32_e32 v42, v42, v49
	s_nop 1
	v_max_f32_dpp v43, v42, v42 quad_perm:[1,0,3,2] row_mask:0xf bank_mask:0xf bound_ctrl:1
	s_nop 1
	v_max_f32_dpp v42, v43, v43 quad_perm:[2,3,0,1] row_mask:0xf bank_mask:0xf bound_ctrl:1
	s_nop 1
	v_max_f32_dpp v43, v42, v42 row_half_mirror row_mask:0xf bank_mask:0xf bound_ctrl:1
	s_nop 1
	v_max_f32_dpp v42, v43, v43 row_mirror row_mask:0xf bank_mask:0xf bound_ctrl:1
	s_nop 1
	v_mov_b32_e32 v43, v42
	s_nop 1
	v_permlane16_swap_b32_e32 v42, v43
	v_max_f32_e32 v42, v42, v43
	v_mov_b32_e32 v43, v42
	s_nop 1
	v_permlane32_swap_b32_e32 v42, v43
	v_max_f32_e32 v49, v42, v43
	v_mul_f32_e32 v44, 0x3b124925, v49
	s_lshl_b32 s11, s4, 2
	s_add_u32 s11, s11, 0x12a00000
	v_mov_b32_e32 v45, s11
	s_mov_b64 exec, 1
	global_store_dword v45, v44, s[6:7]
	s_mov_b64 exec, -1
	v_mov_b32_e32 v46, 0x43e00000
	v_div_scale_f32 v42, s[100:101], v49, v49, v46
	v_rcp_f32_e32 v43, v42
	s_nop 0
	v_fma_f32 v44, -v42, v43, 1.0
	v_fmac_f32_e32 v43, v44, v43
	v_div_scale_f32 v44, vcc, v46, v49, v46
	v_mul_f32_e32 v45, v44, v43
	v_fma_f32 v47, -v42, v45, v44
	v_fmac_f32_e32 v45, v47, v43
	v_fma_f32 v42, -v42, v45, v44
	s_nop 1
	v_div_fmas_f32 v42, v42, v43, v45
	v_div_fixup_f32 v42, v42, v49, v46
	v_cmp_lt_f32_e32 vcc, 0, v49
	s_nop 1
	v_cndmask_b32_e32 v48, 0, v42, vcc
	v_mul_f32_e32 v8, v8, v48
	v_mul_f32_e32 v9, v9, v48
	v_mul_f32_e32 v10, v10, v48
	v_mul_f32_e32 v11, v11, v48
	v_mul_f32_e32 v12, v12, v48
	v_mul_f32_e32 v13, v13, v48
	v_mul_f32_e32 v14, v14, v48
	v_mul_f32_e32 v15, v15, v48
	v_mul_f32_e32 v16, v16, v48
	v_mul_f32_e32 v17, v17, v48
	v_mul_f32_e32 v18, v18, v48
	v_mul_f32_e32 v19, v19, v48
	v_mul_f32_e32 v20, v20, v48
	v_mul_f32_e32 v21, v21, v48
	v_mul_f32_e32 v22, v22, v48
	v_mul_f32_e32 v23, v23, v48
	v_mul_f32_e32 v24, v24, v48
	v_mul_f32_e32 v25, v25, v48
	v_mul_f32_e32 v26, v26, v48
	v_mul_f32_e32 v27, v27, v48
	v_mul_f32_e32 v28, v28, v48
	v_mul_f32_e32 v29, v29, v48
	v_mul_f32_e32 v30, v30, v48
	v_mul_f32_e32 v31, v31, v48
	v_mul_f32_e32 v32, v32, v48
	v_mul_f32_e32 v33, v33, v48
	v_mul_f32_e32 v34, v34, v48
	v_mul_f32_e32 v35, v35, v48
	v_mul_f32_e32 v36, v36, v48
	v_mul_f32_e32 v37, v37, v48
	v_mul_f32_e32 v38, v38, v48
	v_mul_f32_e32 v39, v39, v48
	v_mov_b32_e32 v58, 0
	v_mov_b32_e32 v59, 0
	v_mov_b32_e32 v60, 0
	v_mov_b32_e32 v61, 0
	v_mov_b32_e32 v62, 0
	v_mov_b32_e32 v63, 0
	v_mov_b32_e32 v64, 0
	v_mov_b32_e32 v65, 0
	v_cvt_pk_fp8_f32 v58, v8, v9
	v_cvt_pk_fp8_f32 v59, v12, v13
	v_cvt_pk_fp8_f32 v60, v16, v17
	v_cvt_pk_fp8_f32 v61, v20, v21
	v_cvt_pk_fp8_f32 v62, v24, v25
	v_cvt_pk_fp8_f32 v63, v28, v29
	v_cvt_pk_fp8_f32 v64, v32, v33
	v_cvt_pk_fp8_f32 v65, v36, v37
	v_cvt_pk_fp8_f32 v58, v10, v11 op_sel:[0,0,1]
	v_cvt_pk_fp8_f32 v59, v14, v15 op_sel:[0,0,1]
	v_cvt_pk_fp8_f32 v60, v18, v19 op_sel:[0,0,1]
	v_cvt_pk_fp8_f32 v61, v22, v23 op_sel:[0,0,1]
	v_cvt_pk_fp8_f32 v62, v26, v27 op_sel:[0,0,1]
	v_cvt_pk_fp8_f32 v63, v30, v31 op_sel:[0,0,1]
	v_cvt_pk_fp8_f32 v64, v34, v35 op_sel:[0,0,1]
	v_cvt_pk_fp8_f32 v65, v38, v39 op_sel:[0,0,1]
	s_and_b32 s11, s4, 0x3fff
	s_lshl_b32 s11, s11, 7
	s_lshr_b32 s101, s4, 14
	s_lshl_b32 s101, s101, 25
	s_add_u32 s11, s11, s101
	v_add_u32_e32 v66, s11, v56
	v_add_u32_e32 v67, 0x400000, v66
	v_add_u32_e32 v68, 0x800000, v66
	v_add_u32_e32 v69, 0xc00000, v66
	v_add_u32_e32 v70, 0x1000000, v66
	v_add_u32_e32 v71, 0x1400000, v66
	v_add_u32_e32 v72, 0x1800000, v66
	v_add_u32_e32 v73, 0x1c00000, v66
	global_store_dword v66, v58, s[6:7]
	global_store_dword v67, v59, s[6:7]
	global_store_dword v68, v60, s[6:7]
	global_store_dword v69, v61, s[6:7]
	global_store_dword v70, v62, s[6:7]
	global_store_dword v71, v63, s[6:7]
	global_store_dword v72, v64, s[6:7]
	global_store_dword v73, v65, s[6:7]
	s_add_u32 s4, s4, s10
	s_cmp_ge_u32 s4, 0x8000
	s_cbranch_scc1 .Ldfu_done
	s_add_u32 s11, s4, s10
	s_min_u32 s11, s11, 0x7fff
	s_mov_b32 s101, s11
	s_lshl_b32 s11, s101, 13
	v_add_u32_e32 v40, s11, v7
	v_add_u32_e32 v41, 0x1000, v40
	global_load_dwordx4 v[8:11], v40, s[8:9] nt
	global_load_dwordx4 v[12:15], v40, s[8:9] offset:1024 nt
	global_load_dwordx4 v[16:19], v40, s[8:9] offset:2048 nt
	global_load_dwordx4 v[20:23], v40, s[8:9] offset:3072 nt
	global_load_dwordx4 v[24:27], v41, s[8:9] nt
	global_load_dwordx4 v[28:31], v41, s[8:9] offset:1024 nt
	global_load_dwordx4 v[32:35], v41, s[8:9] offset:2048 nt
	global_load_dwordx4 v[36:39], v41, s[8:9] offset:3072 nt
	s_waitcnt vmcnt(8)
	v_max3_f32 v42, |v76|, |v77|, |v78|
	v_max3_f32 v43, |v80|, |v81|, |v82|
	v_max3_f32 v44, |v84|, |v85|, |v86|
	v_max3_f32 v45, |v88|, |v89|, |v90|
	v_max3_f32 v46, |v92|, |v93|, |v94|
	v_max3_f32 v47, |v96|, |v97|, |v98|
	v_max3_f32 v48, |v100|, |v101|, |v102|
	v_max3_f32 v49, |v104|, |v105|, |v106|
	v_max_f32_e64 v42, v42, |v79|
	v_max_f32_e64 v43, v43, |v83|
	v_max_f32_e64 v44, v44, |v87|
	v_max_f32_e64 v45, v45, |v91|
	v_max_f32_e64 v46, v46, |v95|
	v_max_f32_e64 v47, v47, |v99|
	v_max_f32_e64 v48, v48, |v103|
	v_max_f32_e64 v49, v49, |v107|
	v_max3_f32 v42, v42, v43, v44
	v_max3_f32 v45, v45, v46, v47
	v_max3_f32 v42, v42, v45, v48
	v_max_f32_e32 v42, v42, v49
	s_nop 1
	v_max_f32_dpp v43, v42, v42 quad_perm:[1,0,3,2] row_mask:0xf bank_mask:0xf bound_ctrl:1
	s_nop 1
	v_max_f32_dpp v42, v43, v43 quad_perm:[2,3,0,1] row_mask:0xf bank_mask:0xf bound_ctrl:1
	s_nop 1
	v_max_f32_dpp v43, v42, v42 row_half_mirror row_mask:0xf bank_mask:0xf bound_ctrl:1
	s_nop 1
	v_max_f32_dpp v42, v43, v43 row_mirror row_mask:0xf bank_mask:0xf bound_ctrl:1
	s_nop 1
	v_mov_b32_e32 v43, v42
	s_nop 1
	v_permlane16_swap_b32_e32 v42, v43
	v_max_f32_e32 v42, v42, v43
	v_mov_b32_e32 v43, v42
	s_nop 1
	v_permlane32_swap_b32_e32 v42, v43
	v_max_f32_e32 v49, v42, v43
	v_mul_f32_e32 v44, 0x3b124925, v49
	s_lshl_b32 s11, s4, 2
	s_add_u32 s11, s11, 0x12a00000
	v_mov_b32_e32 v45, s11
	s_mov_b64 exec, 1
	global_store_dword v45, v44, s[6:7]
	s_mov_b64 exec, -1
	v_mov_b32_e32 v46, 0x43e00000
	v_div_scale_f32 v42, s[100:101], v49, v49, v46
	v_rcp_f32_e32 v43, v42
	s_nop 0
	v_fma_f32 v44, -v42, v43, 1.0
	v_fmac_f32_e32 v43, v44, v43
	v_div_scale_f32 v44, vcc, v46, v49, v46
	v_mul_f32_e32 v45, v44, v43
	v_fma_f32 v47, -v42, v45, v44
	v_fmac_f32_e32 v45, v47, v43
	v_fma_f32 v42, -v42, v45, v44
	s_nop 1
	v_div_fmas_f32 v42, v42, v43, v45
	v_div_fixup_f32 v42, v42, v49, v46
	v_cmp_lt_f32_e32 vcc, 0, v49
	s_nop 1
	v_cndmask_b32_e32 v48, 0, v42, vcc
	v_mul_f32_e32 v76, v76, v48
	v_mul_f32_e32 v77, v77, v48
	v_mul_f32_e32 v78, v78, v48
	v_mul_f32_e32 v79, v79, v48
	v_mul_f32_e32 v80, v80, v48
	v_mul_f32_e32 v81, v81, v48
	v_mul_f32_e32 v82, v82, v48
	v_mul_f32_e32 v83, v83, v48
	v_mul_f32_e32 v84, v84, v48
	v_mul_f32_e32 v85, v85, v48
	v_mul_f32_e32 v86, v86, v48
	v_mul_f32_e32 v87, v87, v48
	v_mul_f32_e32 v88, v88, v48
	v_mul_f32_e32 v89, v89, v48
	v_mul_f32_e32 v90, v90, v48
	v_mul_f32_e32 v91, v91, v48
	v_mul_f32_e32 v92, v92, v48
	v_mul_f32_e32 v93, v93, v48
	v_mul_f32_e32 v94, v94, v48
	v_mul_f32_e32 v95, v95, v48
	v_mul_f32_e32 v96, v96, v48
	v_mul_f32_e32 v97, v97, v48
	v_mul_f32_e32 v98, v98, v48
	v_mul_f32_e32 v99, v99, v48
	v_mul_f32_e32 v100, v100, v48
	v_mul_f32_e32 v101, v101, v48
	v_mul_f32_e32 v102, v102, v48
	v_mul_f32_e32 v103, v103, v48
	v_mul_f32_e32 v104, v104, v48
	v_mul_f32_e32 v105, v105, v48
	v_mul_f32_e32 v106, v106, v48
	v_mul_f32_e32 v107, v107, v48
	v_mov_b32_e32 v58, 0
	v_mov_b32_e32 v59, 0
	v_mov_b32_e32 v60, 0
	v_mov_b32_e32 v61, 0
	v_mov_b32_e32 v62, 0
	v_mov_b32_e32 v63, 0
	v_mov_b32_e32 v64, 0
	v_mov_b32_e32 v65, 0
	v_cvt_pk_fp8_f32 v58, v76, v77
	v_cvt_pk_fp8_f32 v59, v80, v81
	v_cvt_pk_fp8_f32 v60, v84, v85
	v_cvt_pk_fp8_f32 v61, v88, v89
	v_cvt_pk_fp8_f32 v62, v92, v93
	v_cvt_pk_fp8_f32 v63, v96, v97
	v_cvt_pk_fp8_f32 v64, v100, v101
	v_cvt_pk_fp8_f32 v65, v104, v105
	v_cvt_pk_fp8_f32 v58, v78, v79 op_sel:[0,0,1]
	v_cvt_pk_fp8_f32 v59, v82, v83 op_sel:[0,0,1]
	v_cvt_pk_fp8_f32 v60, v86, v87 op_sel:[0,0,1]
	v_cvt_pk_fp8_f32 v61, v90, v91 op_sel:[0,0,1]
	v_cvt_pk_fp8_f32 v62, v94, v95 op_sel:[0,0,1]
	v_cvt_pk_fp8_f32 v63, v98, v99 op_sel:[0,0,1]
	v_cvt_pk_fp8_f32 v64, v102, v103 op_sel:[0,0,1]
	v_cvt_pk_fp8_f32 v65, v106, v107 op_sel:[0,0,1]
	s_and_b32 s11, s4, 0x3fff
	s_lshl_b32 s11, s11, 7
	s_lshr_b32 s101, s4, 14
	s_lshl_b32 s101, s101, 25
	s_add_u32 s11, s11, s101
	v_add_u32_e32 v66, s11, v56
	v_add_u32_e32 v67, 0x400000, v66
	v_add_u32_e32 v68, 0x800000, v66
	v_add_u32_e32 v69, 0xc00000, v66
	v_add_u32_e32 v70, 0x1000000, v66
	v_add_u32_e32 v71, 0x1400000, v66
	v_add_u32_e32 v72, 0x1800000, v66
	v_add_u32_e32 v73, 0x1c00000, v66
	global_store_dword v66, v58, s[6:7]
	global_store_dword v67, v59, s[6:7]
	global_store_dword v68, v60, s[6:7]
	global_store_dword v69, v61, s[6:7]
	global_store_dword v70, v62, s[6:7]
	global_store_dword v71, v63, s[6:7]
	global_store_dword v72, v64, s[6:7]
	global_store_dword v73, v65, s[6:7]
	s_add_u32 s4, s4, s10
	s_cmp_ge_u32 s4, 0x8000
	s_cbranch_scc1 .Ldfu_done
	s_branch .Ldfu_loop

.LBB0_709:
	v_readlane_b32 s4, v255, 36
	v_readlane_b32 s8, v252, 0
	s_add_i32 s5, s4, 8
	v_readlane_b32 s9, v252, 1
	s_cmp_ge_i32 s5, s9
	v_readlane_b32 s10, v252, 2
	v_readlane_b32 s11, v252, 3
	s_cbranch_scc1 .LBB0_721
	v_readlane_b32 s4, v255, 34
	s_nop 0
	s_cmp_lg_u32 s4, 0
	s_cbranch_scc1 .Ldfv0_done
	s_cmp_gt_u32 s82, 32
	s_cselect_b32 s11, 32, 0
	s_cmp_lt_u32 s2, s11
	s_cbranch_scc1 .Ldfv0_done
	s_sub_u32 s10, s82, s11
	s_lshl_b32 s10, s10, 3
	s_sub_u32 s4, s2, s11
	s_lshl_b32 s4, s4, 3
	v_readfirstlane_b32 s11, v0
	s_lshr_b32 s11, s11, 6
	s_add_u32 s4, s4, s11
	s_add_u32 s4, s4, 0x0
	s_cmp_ge_u32 s4, 0x4000
	s_cbranch_scc1 .Ldfv0_done
	v_readlane_b32 s6, v252, 4
	v_readlane_b32 s7, v252, 5
	s_nop 0
	s_sub_u32 s6, s6, 0x38
	s_subb_u32 s7, s7, 0
	s_load_dwordx2 s[8:9], s[6:7], 0x8
	s_load_dwordx2 s[6:7], s[6:7], 0x20
	v_and_b32_e32 v6, 63, v0
	v_lshlrev_b32_e32 v7, 4, v6
	v_lshrrev_b32_e32 v56, 5, v6
	v_and_b32_e32 v57, 31, v6
	v_lshlrev_b32_e32 v56, 21, v56
	v_lshl_add_u32 v56, v57, 2, v56
	v_add_u32_e32 v56, 0xea00000, v56
	s_mov_b64 exec, -1
	s_waitcnt lgkmcnt(0)
	s_lshl_b32 s11, s4, 13
	v_add_u32_e32 v40, s11, v7
	v_add_u32_e32 v41, 0x1000, v40
	global_load_dwordx4 v[8:11], v40, s[8:9] nt
	global_load_dwordx4 v[12:15], v40, s[8:9] offset:1024 nt
	global_load_dwordx4 v[16:19], v40, s[8:9] offset:2048 nt
	global_load_dwordx4 v[20:23], v40, s[8:9] offset:3072 nt
	global_load_dwordx4 v[24:27], v41, s[8:9] nt
	global_load_dwordx4 v[28:31], v41, s[8:9] offset:1024 nt
	global_load_dwordx4 v[32:35], v41, s[8:9] offset:2048 nt
	global_load_dwordx4 v[36:39], v41, s[8:9] offset:3072 nt
.Ldfv0_loop:
	s_add_u32 s11, s4, s10
	s_min_u32 s11, s11, 0x3fff
	s_mov_b32 s101, s11
	s_lshl_b32 s11, s101, 13
	v_add_u32_e32 v40, s11, v7
	v_add_u32_e32 v41, 0x1000, v40
	global_load_dwordx4 v[76:79], v40, s[8:9] nt
	global_load_dwordx4 v[80:83], v40, s[8:9] offset:1024 nt
	global_load_dwordx4 v[84:87], v40, s[8:9] offset:2048 nt
	global_load_dwordx4 v[88:91], v40, s[8:9] offset:3072 nt
	global_load_dwordx4 v[92:95], v41, s[8:9] nt
	global_load_dwordx4 v[96:99], v41, s[8:9] offset:1024 nt
	global_load_dwordx4 v[100:103], v41, s[8:9] offset:2048 nt
	global_load_dwordx4 v[104:107], v41, s[8:9] offset:3072 nt
	s_waitcnt vmcnt(8)
	v_max3_f32 v42, |v8|, |v9|, |v10|
	v_max3_f32 v43, |v12|, |v13|, |v14|
	v_max3_f32 v44, |v16|, |v17|, |v18|
	v_max3_f32 v45, |v20|, |v21|, |v22|
	v_max3_f32 v46, |v24|, |v25|, |v26|
	v_max3_f32 v47, |v28|, |v29|, |v30|
	v_max3_f32 v48, |v32|, |v33|, |v34|
	v_max3_f32 v49, |v36|, |v37|, |v38|
	v_max_f32_e64 v42, v42, |v11|
	v_max_f32_e64 v43, v43, |v15|
	v_max_f32_e64 v44, v44, |v19|
	v_max_f32_e64 v45, v45, |v23|
	v_max_f32_e64 v46, v46, |v27|
	v_max_f32_e64 v47, v47, |v31|
	v_max_f32_e64 v48, v48, |v35|
	v_max_f32_e64 v49, v49, |v39|
	v_max3_f32 v42, v42, v43, v44
	v_max3_f32 v45, v45, v46, v47
	v_max3_f32 v42, v42, v45, v48
	v_max_f32_e32 v42, v42, v49
	s_nop 1
	v_max_f32_dpp v43, v42, v42 quad_perm:[1,0,3,2] row_mask:0xf bank_mask:0xf bound_ctrl:1
	s_nop 1
	v_max_f32_dpp v42, v43, v43 quad_perm:[2,3,0,1] row_mask:0xf bank_mask:0xf bound_ctrl:1
	s_nop 1
	v_max_f32_dpp v43, v42, v42 row_half_mirror row_mask:0xf bank_mask:0xf bound_ctrl:1
	s_nop 1
	v_max_f32_dpp v42, v43, v43 row_mirror row_mask:0xf bank_mask:0xf bound_ctrl:1
	s_nop 1
	v_mov_b32_e32 v43, v42
	s_nop 1
	v_permlane16_swap_b32_e32 v42, v43
	v_max_f32_e32 v42, v42, v43
	v_mov_b32_e32 v43, v42
	s_nop 1
	v_permlane32_swap_b32_e32 v42, v43
	v_max_f32_e32 v49, v42, v43
	v_mul_f32_e32 v44, 0x3b124925, v49
	s_lshl_b32 s11, s4, 2
	s_add_u32 s11, s11, 0x12a20000
	v_mov_b32_e32 v45, s11
	s_mov_b64 exec, 1
	global_store_dword v45, v44, s[6:7]
	s_mov_b64 exec, -1
	v_mov_b32_e32 v46, 0x43e00000
	v_div_scale_f32 v42, s[100:101], v49, v49, v46
	v_rcp_f32_e32 v43, v42
	s_nop 0
	v_fma_f32 v44, -v42, v43, 1.0
	v_fmac_f32_e32 v43, v44, v43
	v_div_scale_f32 v44, vcc, v46, v49, v46
	v_mul_f32_e32 v45, v44, v43
	v_fma_f32 v47, -v42, v45, v44
	v_fmac_f32_e32 v45, v47, v43
	v_fma_f32 v42, -v42, v45, v44
	s_nop 1
	v_div_fmas_f32 v42, v42, v43, v45
	v_div_fixup_f32 v42, v42, v49, v46
	v_cmp_lt_f32_e32 vcc, 0, v49
	s_nop 1
	v_cndmask_b32_e32 v48, 0, v42, vcc
	v_mul_f32_e32 v8, v8, v48
	v_mul_f32_e32 v9, v9, v48
	v_mul_f32_e32 v10, v10, v48
	v_mul_f32_e32 v11, v11, v48
	v_mul_f32_e32 v12, v12, v48
	v_mul_f32_e32 v13, v13, v48
	v_mul_f32_e32 v14, v14, v48
	v_mul_f32_e32 v15, v15, v48
	v_mul_f32_e32 v16, v16, v48
	v_mul_f32_e32 v17, v17, v48
	v_mul_f32_e32 v18, v18, v48
	v_mul_f32_e32 v19, v19, v48
	v_mul_f32_e32 v20, v20, v48
	v_mul_f32_e32 v21, v21, v48
	v_mul_f32_e32 v22, v22, v48
	v_mul_f32_e32 v23, v23, v48
	v_mul_f32_e32 v24, v24, v48
	v_mul_f32_e32 v25, v25, v48
	v_mul_f32_e32 v26, v26, v48
	v_mul_f32_e32 v27, v27, v48
	v_mul_f32_e32 v28, v28, v48
	v_mul_f32_e32 v29, v29, v48
	v_mul_f32_e32 v30, v30, v48
	v_mul_f32_e32 v31, v31, v48
	v_mul_f32_e32 v32, v32, v48
	v_mul_f32_e32 v33, v33, v48
	v_mul_f32_e32 v34, v34, v48
	v_mul_f32_e32 v35, v35, v48
	v_mul_f32_e32 v36, v36, v48
	v_mul_f32_e32 v37, v37, v48
	v_mul_f32_e32 v38, v38, v48
	v_mul_f32_e32 v39, v39, v48
	v_mov_b32_e32 v58, 0
	v_mov_b32_e32 v59, 0
	v_mov_b32_e32 v60, 0
	v_mov_b32_e32 v61, 0
	v_mov_b32_e32 v62, 0
	v_mov_b32_e32 v63, 0
	v_mov_b32_e32 v64, 0
	v_mov_b32_e32 v65, 0
	v_cvt_pk_fp8_f32 v58, v8, v9
	v_cvt_pk_fp8_f32 v59, v12, v13
	v_cvt_pk_fp8_f32 v60, v16, v17
	v_cvt_pk_fp8_f32 v61, v20, v21
	v_cvt_pk_fp8_f32 v62, v24, v25
	v_cvt_pk_fp8_f32 v63, v28, v29
	v_cvt_pk_fp8_f32 v64, v32, v33
	v_cvt_pk_fp8_f32 v65, v36, v37
	v_cvt_pk_fp8_f32 v58, v10, v11 op_sel:[0,0,1]
	v_cvt_pk_fp8_f32 v59, v14, v15 op_sel:[0,0,1]
	v_cvt_pk_fp8_f32 v60, v18, v19 op_sel:[0,0,1]
	v_cvt_pk_fp8_f32 v61, v22, v23 op_sel:[0,0,1]
	v_cvt_pk_fp8_f32 v62, v26, v27 op_sel:[0,0,1]
	v_cvt_pk_fp8_f32 v63, v30, v31 op_sel:[0,0,1]
	v_cvt_pk_fp8_f32 v64, v34, v35 op_sel:[0,0,1]
	v_cvt_pk_fp8_f32 v65, v38, v39 op_sel:[0,0,1]
	s_and_b32 s11, s4, 0x3fff
	s_lshl_b32 s11, s11, 7
	s_lshr_b32 s101, s4, 14
	s_lshl_b32 s101, s101, 25
	s_add_u32 s11, s11, s101
	v_add_u32_e32 v66, s11, v56
	v_add_u32_e32 v67, 0x400000, v66
	v_add_u32_e32 v68, 0x800000, v66
	v_add_u32_e32 v69, 0xc00000, v66
	v_add_u32_e32 v70, 0x1000000, v66
	v_add_u32_e32 v71, 0x1400000, v66
	v_add_u32_e32 v72, 0x1800000, v66
	v_add_u32_e32 v73, 0x1c00000, v66
	global_store_dword v66, v58, s[6:7]
	global_store_dword v67, v59, s[6:7]
	global_store_dword v68, v60, s[6:7]
	global_store_dword v69, v61, s[6:7]
	global_store_dword v70, v62, s[6:7]
	global_store_dword v71, v63, s[6:7]
	global_store_dword v72, v64, s[6:7]
	global_store_dword v73, v65, s[6:7]
	s_add_u32 s4, s4, s10
	s_cmp_ge_u32 s4, 0x4000
	s_cbranch_scc1 .Ldfv0_done
	s_add_u32 s11, s4, s10
	s_min_u32 s11, s11, 0x3fff
	s_mov_b32 s101, s11
	s_lshl_b32 s11, s101, 13
	v_add_u32_e32 v40, s11, v7
	v_add_u32_e32 v41, 0x1000, v40
	global_load_dwordx4 v[8:11], v40, s[8:9] nt
	global_load_dwordx4 v[12:15], v40, s[8:9] offset:1024 nt
	global_load_dwordx4 v[16:19], v40, s[8:9] offset:2048 nt
	global_load_dwordx4 v[20:23], v40, s[8:9] offset:3072 nt
	global_load_dwordx4 v[24:27], v41, s[8:9] nt
	global_load_dwordx4 v[28:31], v41, s[8:9] offset:1024 nt
	global_load_dwordx4 v[32:35], v41, s[8:9] offset:2048 nt
	global_load_dwordx4 v[36:39], v41, s[8:9] offset:3072 nt
	s_waitcnt vmcnt(8)
	v_max3_f32 v42, |v76|, |v77|, |v78|
	v_max3_f32 v43, |v80|, |v81|, |v82|
	v_max3_f32 v44, |v84|, |v85|, |v86|
	v_max3_f32 v45, |v88|, |v89|, |v90|
	v_max3_f32 v46, |v92|, |v93|, |v94|
	v_max3_f32 v47, |v96|, |v97|, |v98|
	v_max3_f32 v48, |v100|, |v101|, |v102|
	v_max3_f32 v49, |v104|, |v105|, |v106|
	v_max_f32_e64 v42, v42, |v79|
	v_max_f32_e64 v43, v43, |v83|
	v_max_f32_e64 v44, v44, |v87|
	v_max_f32_e64 v45, v45, |v91|
	v_max_f32_e64 v46, v46, |v95|
	v_max_f32_e64 v47, v47, |v99|
	v_max_f32_e64 v48, v48, |v103|
	v_max_f32_e64 v49, v49, |v107|
	v_max3_f32 v42, v42, v43, v44
	v_max3_f32 v45, v45, v46, v47
	v_max3_f32 v42, v42, v45, v48
	v_max_f32_e32 v42, v42, v49
	s_nop 1
	v_max_f32_dpp v43, v42, v42 quad_perm:[1,0,3,2] row_mask:0xf bank_mask:0xf bound_ctrl:1
	s_nop 1
	v_max_f32_dpp v42, v43, v43 quad_perm:[2,3,0,1] row_mask:0xf bank_mask:0xf bound_ctrl:1
	s_nop 1
	v_max_f32_dpp v43, v42, v42 row_half_mirror row_mask:0xf bank_mask:0xf bound_ctrl:1
	s_nop 1
	v_max_f32_dpp v42, v43, v43 row_mirror row_mask:0xf bank_mask:0xf bound_ctrl:1
	s_nop 1
	v_mov_b32_e32 v43, v42
	s_nop 1
	v_permlane16_swap_b32_e32 v42, v43
	v_max_f32_e32 v42, v42, v43
	v_mov_b32_e32 v43, v42
	s_nop 1
	v_permlane32_swap_b32_e32 v42, v43
	v_max_f32_e32 v49, v42, v43
	v_mul_f32_e32 v44, 0x3b124925, v49
	s_lshl_b32 s11, s4, 2
	s_add_u32 s11, s11, 0x12a20000
	v_mov_b32_e32 v45, s11
	s_mov_b64 exec, 1
	global_store_dword v45, v44, s[6:7]
	s_mov_b64 exec, -1
	v_mov_b32_e32 v46, 0x43e00000
	v_div_scale_f32 v42, s[100:101], v49, v49, v46
	v_rcp_f32_e32 v43, v42
	s_nop 0
	v_fma_f32 v44, -v42, v43, 1.0
	v_fmac_f32_e32 v43, v44, v43
	v_div_scale_f32 v44, vcc, v46, v49, v46
	v_mul_f32_e32 v45, v44, v43
	v_fma_f32 v47, -v42, v45, v44
	v_fmac_f32_e32 v45, v47, v43
	v_fma_f32 v42, -v42, v45, v44
	s_nop 1
	v_div_fmas_f32 v42, v42, v43, v45
	v_div_fixup_f32 v42, v42, v49, v46
	v_cmp_lt_f32_e32 vcc, 0, v49
	s_nop 1
	v_cndmask_b32_e32 v48, 0, v42, vcc
	v_mul_f32_e32 v76, v76, v48
	v_mul_f32_e32 v77, v77, v48
	v_mul_f32_e32 v78, v78, v48
	v_mul_f32_e32 v79, v79, v48
	v_mul_f32_e32 v80, v80, v48
	v_mul_f32_e32 v81, v81, v48
	v_mul_f32_e32 v82, v82, v48
	v_mul_f32_e32 v83, v83, v48
	v_mul_f32_e32 v84, v84, v48
	v_mul_f32_e32 v85, v85, v48
	v_mul_f32_e32 v86, v86, v48
	v_mul_f32_e32 v87, v87, v48
	v_mul_f32_e32 v88, v88, v48
	v_mul_f32_e32 v89, v89, v48
	v_mul_f32_e32 v90, v90, v48
	v_mul_f32_e32 v91, v91, v48
	v_mul_f32_e32 v92, v92, v48
	v_mul_f32_e32 v93, v93, v48
	v_mul_f32_e32 v94, v94, v48
	v_mul_f32_e32 v95, v95, v48
	v_mul_f32_e32 v96, v96, v48
	v_mul_f32_e32 v97, v97, v48
	v_mul_f32_e32 v98, v98, v48
	v_mul_f32_e32 v99, v99, v48
	v_mul_f32_e32 v100, v100, v48
	v_mul_f32_e32 v101, v101, v48
	v_mul_f32_e32 v102, v102, v48
	v_mul_f32_e32 v103, v103, v48
	v_mul_f32_e32 v104, v104, v48
	v_mul_f32_e32 v105, v105, v48
	v_mul_f32_e32 v106, v106, v48
	v_mul_f32_e32 v107, v107, v48
	v_mov_b32_e32 v58, 0
	v_mov_b32_e32 v59, 0
	v_mov_b32_e32 v60, 0
	v_mov_b32_e32 v61, 0
	v_mov_b32_e32 v62, 0
	v_mov_b32_e32 v63, 0
	v_mov_b32_e32 v64, 0
	v_mov_b32_e32 v65, 0
	v_cvt_pk_fp8_f32 v58, v76, v77
	v_cvt_pk_fp8_f32 v59, v80, v81
	v_cvt_pk_fp8_f32 v60, v84, v85
	v_cvt_pk_fp8_f32 v61, v88, v89
	v_cvt_pk_fp8_f32 v62, v92, v93
	v_cvt_pk_fp8_f32 v63, v96, v97
	v_cvt_pk_fp8_f32 v64, v100, v101
	v_cvt_pk_fp8_f32 v65, v104, v105
	v_cvt_pk_fp8_f32 v58, v78, v79 op_sel:[0,0,1]
	v_cvt_pk_fp8_f32 v59, v82, v83 op_sel:[0,0,1]
	v_cvt_pk_fp8_f32 v60, v86, v87 op_sel:[0,0,1]
	v_cvt_pk_fp8_f32 v61, v90, v91 op_sel:[0,0,1]
	v_cvt_pk_fp8_f32 v62, v94, v95 op_sel:[0,0,1]
	v_cvt_pk_fp8_f32 v63, v98, v99 op_sel:[0,0,1]
	v_cvt_pk_fp8_f32 v64, v102, v103 op_sel:[0,0,1]
	v_cvt_pk_fp8_f32 v65, v106, v107 op_sel:[0,0,1]
	s_and_b32 s11, s4, 0x3fff
	s_lshl_b32 s11, s11, 7
	s_lshr_b32 s101, s4, 14
	s_lshl_b32 s101, s101, 25
	s_add_u32 s11, s11, s101
	v_add_u32_e32 v66, s11, v56
	v_add_u32_e32 v67, 0x400000, v66
	v_add_u32_e32 v68, 0x800000, v66
	v_add_u32_e32 v69, 0xc00000, v66
	v_add_u32_e32 v70, 0x1000000, v66
	v_add_u32_e32 v71, 0x1400000, v66
	v_add_u32_e32 v72, 0x1800000, v66
	v_add_u32_e32 v73, 0x1c00000, v66
	global_store_dword v66, v58, s[6:7]
	global_store_dword v67, v59, s[6:7]
	global_store_dword v68, v60, s[6:7]
	global_store_dword v69, v61, s[6:7]
	global_store_dword v70, v62, s[6:7]
	global_store_dword v71, v63, s[6:7]
	global_store_dword v72, v64, s[6:7]
	global_store_dword v73, v65, s[6:7]
	s_add_u32 s4, s4, s10
	s_cmp_ge_u32 s4, 0x4000
	s_cbranch_scc1 .Ldfv0_done
	s_branch .Ldfv0_loop

.LBB0_856:
	v_readlane_b32 s4, v255, 36
	v_readlane_b32 s8, v252, 0
	s_add_i32 s5, s4, 10
	v_readlane_b32 s9, v252, 1
	s_cmp_ge_i32 s5, s9
	v_readlane_b32 s10, v252, 2
	v_readlane_b32 s11, v252, 3
	s_cbranch_scc1 .LBB0_906
	v_readlane_b32 s4, v255, 34
	s_nop 0
	s_cmp_lg_u32 s4, 0
	s_cbranch_scc1 .Ldfv1_done
	s_cmp_gt_u32 s82, 32
	s_cselect_b32 s11, 32, 0
	s_cmp_lt_u32 s2, s11
	s_cbranch_scc1 .Ldfv1_done
	s_sub_u32 s10, s82, s11
	s_lshl_b32 s10, s10, 3
	s_sub_u32 s4, s2, s11
	s_lshl_b32 s4, s4, 3
	v_readfirstlane_b32 s11, v0
	s_lshr_b32 s11, s11, 6
	s_add_u32 s4, s4, s11
	s_add_u32 s4, s4, 0x4000
	s_cmp_ge_u32 s4, 0x8000
	s_cbranch_scc1 .Ldfv1_done
	v_readlane_b32 s6, v252, 4
	v_readlane_b32 s7, v252, 5
	s_nop 0
	s_sub_u32 s6, s6, 0x38
	s_subb_u32 s7, s7, 0
	s_load_dwordx2 s[8:9], s[6:7], 0x8
	s_load_dwordx2 s[6:7], s[6:7], 0x20
	v_and_b32_e32 v6, 63, v0
	v_lshlrev_b32_e32 v7, 4, v6
	v_lshrrev_b32_e32 v56, 5, v6
	v_and_b32_e32 v57, 31, v6
	v_lshlrev_b32_e32 v56, 21, v56
	v_lshl_add_u32 v56, v57, 2, v56
	v_add_u32_e32 v56, 0xea00000, v56
	s_mov_b64 exec, -1
	s_waitcnt lgkmcnt(0)
	s_lshl_b32 s11, s4, 13
	v_add_u32_e32 v40, s11, v7
	v_add_u32_e32 v41, 0x1000, v40
	global_load_dwordx4 v[8:11], v40, s[8:9] nt
	global_load_dwordx4 v[12:15], v40, s[8:9] offset:1024 nt
	global_load_dwordx4 v[16:19], v40, s[8:9] offset:2048 nt
	global_load_dwordx4 v[20:23], v40, s[8:9] offset:3072 nt
	global_load_dwordx4 v[24:27], v41, s[8:9] nt
	global_load_dwordx4 v[28:31], v41, s[8:9] offset:1024 nt
	global_load_dwordx4 v[32:35], v41, s[8:9] offset:2048 nt
	global_load_dwordx4 v[36:39], v41, s[8:9] offset:3072 nt
.Ldfv1_loop:
	s_add_u32 s11, s4, s10
	s_min_u32 s11, s11, 0x7fff
	s_mov_b32 s101, s11
	s_lshl_b32 s11, s101, 13
	v_add_u32_e32 v40, s11, v7
	v_add_u32_e32 v41, 0x1000, v40
	global_load_dwordx4 v[76:79], v40, s[8:9] nt
	global_load_dwordx4 v[80:83], v40, s[8:9] offset:1024 nt
	global_load_dwordx4 v[84:87], v40, s[8:9] offset:2048 nt
	global_load_dwordx4 v[88:91], v40, s[8:9] offset:3072 nt
	global_load_dwordx4 v[92:95], v41, s[8:9] nt
	global_load_dwordx4 v[96:99], v41, s[8:9] offset:1024 nt
	global_load_dwordx4 v[100:103], v41, s[8:9] offset:2048 nt
	global_load_dwordx4 v[104:107], v41, s[8:9] offset:3072 nt
	s_waitcnt vmcnt(8)
	v_max3_f32 v42, |v8|, |v9|, |v10|
	v_max3_f32 v43, |v12|, |v13|, |v14|
	v_max3_f32 v44, |v16|, |v17|, |v18|
	v_max3_f32 v45, |v20|, |v21|, |v22|
	v_max3_f32 v46, |v24|, |v25|, |v26|
	v_max3_f32 v47, |v28|, |v29|, |v30|
	v_max3_f32 v48, |v32|, |v33|, |v34|
	v_max3_f32 v49, |v36|, |v37|, |v38|
	v_max_f32_e64 v42, v42, |v11|
	v_max_f32_e64 v43, v43, |v15|
	v_max_f32_e64 v44, v44, |v19|
	v_max_f32_e64 v45, v45, |v23|
	v_max_f32_e64 v46, v46, |v27|
	v_max_f32_e64 v47, v47, |v31|
	v_max_f32_e64 v48, v48, |v35|
	v_max_f32_e64 v49, v49, |v39|
	v_max3_f32 v42, v42, v43, v44
	v_max3_f32 v45, v45, v46, v47
	v_max3_f32 v42, v42, v45, v48
	v_max_f32_e32 v42, v42, v49
	s_nop 1
	v_max_f32_dpp v43, v42, v42 quad_perm:[1,0,3,2] row_mask:0xf bank_mask:0xf bound_ctrl:1
	s_nop 1
	v_max_f32_dpp v42, v43, v43 quad_perm:[2,3,0,1] row_mask:0xf bank_mask:0xf bound_ctrl:1
	s_nop 1
	v_max_f32_dpp v43, v42, v42 row_half_mirror row_mask:0xf bank_mask:0xf bound_ctrl:1
	s_nop 1
	v_max_f32_dpp v42, v43, v43 row_mirror row_mask:0xf bank_mask:0xf bound_ctrl:1
	s_nop 1
	v_mov_b32_e32 v43, v42
	s_nop 1
	v_permlane16_swap_b32_e32 v42, v43
	v_max_f32_e32 v42, v42, v43
	v_mov_b32_e32 v43, v42
	s_nop 1
	v_permlane32_swap_b32_e32 v42, v43
	v_max_f32_e32 v49, v42, v43
	v_mul_f32_e32 v44, 0x3b124925, v49
	s_lshl_b32 s11, s4, 2
	s_add_u32 s11, s11, 0x12a20000
	v_mov_b32_e32 v45, s11
	s_mov_b64 exec, 1
	global_store_dword v45, v44, s[6:7]
	s_mov_b64 exec, -1
	v_mov_b32_e32 v46, 0x43e00000
	v_div_scale_f32 v42, s[100:101], v49, v49, v46
	v_rcp_f32_e32 v43, v42
	s_nop 0
	v_fma_f32 v44, -v42, v43, 1.0
	v_fmac_f32_e32 v43, v44, v43
	v_div_scale_f32 v44, vcc, v46, v49, v46
	v_mul_f32_e32 v45, v44, v43
	v_fma_f32 v47, -v42, v45, v44
	v_fmac_f32_e32 v45, v47, v43
	v_fma_f32 v42, -v42, v45, v44
	s_nop 1
	v_div_fmas_f32 v42, v42, v43, v45
	v_div_fixup_f32 v42, v42, v49, v46
	v_cmp_lt_f32_e32 vcc, 0, v49
	s_nop 1
	v_cndmask_b32_e32 v48, 0, v42, vcc
	v_mul_f32_e32 v8, v8, v48
	v_mul_f32_e32 v9, v9, v48
	v_mul_f32_e32 v10, v10, v48
	v_mul_f32_e32 v11, v11, v48
	v_mul_f32_e32 v12, v12, v48
	v_mul_f32_e32 v13, v13, v48
	v_mul_f32_e32 v14, v14, v48
	v_mul_f32_e32 v15, v15, v48
	v_mul_f32_e32 v16, v16, v48
	v_mul_f32_e32 v17, v17, v48
	v_mul_f32_e32 v18, v18, v48
	v_mul_f32_e32 v19, v19, v48
	v_mul_f32_e32 v20, v20, v48
	v_mul_f32_e32 v21, v21, v48
	v_mul_f32_e32 v22, v22, v48
	v_mul_f32_e32 v23, v23, v48
	v_mul_f32_e32 v24, v24, v48
	v_mul_f32_e32 v25, v25, v48
	v_mul_f32_e32 v26, v26, v48
	v_mul_f32_e32 v27, v27, v48
	v_mul_f32_e32 v28, v28, v48
	v_mul_f32_e32 v29, v29, v48
	v_mul_f32_e32 v30, v30, v48
	v_mul_f32_e32 v31, v31, v48
	v_mul_f32_e32 v32, v32, v48
	v_mul_f32_e32 v33, v33, v48
	v_mul_f32_e32 v34, v34, v48
	v_mul_f32_e32 v35, v35, v48
	v_mul_f32_e32 v36, v36, v48
	v_mul_f32_e32 v37, v37, v48
	v_mul_f32_e32 v38, v38, v48
	v_mul_f32_e32 v39, v39, v48
	v_mov_b32_e32 v58, 0
	v_mov_b32_e32 v59, 0
	v_mov_b32_e32 v60, 0
	v_mov_b32_e32 v61, 0
	v_mov_b32_e32 v62, 0
	v_mov_b32_e32 v63, 0
	v_mov_b32_e32 v64, 0
	v_mov_b32_e32 v65, 0
	v_cvt_pk_fp8_f32 v58, v8, v9
	v_cvt_pk_fp8_f32 v59, v12, v13
	v_cvt_pk_fp8_f32 v60, v16, v17
	v_cvt_pk_fp8_f32 v61, v20, v21
	v_cvt_pk_fp8_f32 v62, v24, v25
	v_cvt_pk_fp8_f32 v63, v28, v29
	v_cvt_pk_fp8_f32 v64, v32, v33
	v_cvt_pk_fp8_f32 v65, v36, v37
	v_cvt_pk_fp8_f32 v58, v10, v11 op_sel:[0,0,1]
	v_cvt_pk_fp8_f32 v59, v14, v15 op_sel:[0,0,1]
	v_cvt_pk_fp8_f32 v60, v18, v19 op_sel:[0,0,1]
	v_cvt_pk_fp8_f32 v61, v22, v23 op_sel:[0,0,1]
	v_cvt_pk_fp8_f32 v62, v26, v27 op_sel:[0,0,1]
	v_cvt_pk_fp8_f32 v63, v30, v31 op_sel:[0,0,1]
	v_cvt_pk_fp8_f32 v64, v34, v35 op_sel:[0,0,1]
	v_cvt_pk_fp8_f32 v65, v38, v39 op_sel:[0,0,1]
	s_and_b32 s11, s4, 0x3fff
	s_lshl_b32 s11, s11, 7
	s_lshr_b32 s101, s4, 14
	s_lshl_b32 s101, s101, 25
	s_add_u32 s11, s11, s101
	v_add_u32_e32 v66, s11, v56
	v_add_u32_e32 v67, 0x400000, v66
	v_add_u32_e32 v68, 0x800000, v66
	v_add_u32_e32 v69, 0xc00000, v66
	v_add_u32_e32 v70, 0x1000000, v66
	v_add_u32_e32 v71, 0x1400000, v66
	v_add_u32_e32 v72, 0x1800000, v66
	v_add_u32_e32 v73, 0x1c00000, v66
	global_store_dword v66, v58, s[6:7]
	global_store_dword v67, v59, s[6:7]
	global_store_dword v68, v60, s[6:7]
	global_store_dword v69, v61, s[6:7]
	global_store_dword v70, v62, s[6:7]
	global_store_dword v71, v63, s[6:7]
	global_store_dword v72, v64, s[6:7]
	global_store_dword v73, v65, s[6:7]
	s_add_u32 s4, s4, s10
	s_cmp_ge_u32 s4, 0x8000
	s_cbranch_scc1 .Ldfv1_done
	s_add_u32 s11, s4, s10
	s_min_u32 s11, s11, 0x7fff
	s_mov_b32 s101, s11
	s_lshl_b32 s11, s101, 13
	v_add_u32_e32 v40, s11, v7
	v_add_u32_e32 v41, 0x1000, v40
	global_load_dwordx4 v[8:11], v40, s[8:9] nt
	global_load_dwordx4 v[12:15], v40, s[8:9] offset:1024 nt
	global_load_dwordx4 v[16:19], v40, s[8:9] offset:2048 nt
	global_load_dwordx4 v[20:23], v40, s[8:9] offset:3072 nt
	global_load_dwordx4 v[24:27], v41, s[8:9] nt
	global_load_dwordx4 v[28:31], v41, s[8:9] offset:1024 nt
	global_load_dwordx4 v[32:35], v41, s[8:9] offset:2048 nt
	global_load_dwordx4 v[36:39], v41, s[8:9] offset:3072 nt
	s_waitcnt vmcnt(8)
	v_max3_f32 v42, |v76|, |v77|, |v78|
	v_max3_f32 v43, |v80|, |v81|, |v82|
	v_max3_f32 v44, |v84|, |v85|, |v86|
	v_max3_f32 v45, |v88|, |v89|, |v90|
	v_max3_f32 v46, |v92|, |v93|, |v94|
	v_max3_f32 v47, |v96|, |v97|, |v98|
	v_max3_f32 v48, |v100|, |v101|, |v102|
	v_max3_f32 v49, |v104|, |v105|, |v106|
	v_max_f32_e64 v42, v42, |v79|
	v_max_f32_e64 v43, v43, |v83|
	v_max_f32_e64 v44, v44, |v87|
	v_max_f32_e64 v45, v45, |v91|
	v_max_f32_e64 v46, v46, |v95|
	v_max_f32_e64 v47, v47, |v99|
	v_max_f32_e64 v48, v48, |v103|
	v_max_f32_e64 v49, v49, |v107|
	v_max3_f32 v42, v42, v43, v44
	v_max3_f32 v45, v45, v46, v47
	v_max3_f32 v42, v42, v45, v48
	v_max_f32_e32 v42, v42, v49
	s_nop 1
	v_max_f32_dpp v43, v42, v42 quad_perm:[1,0,3,2] row_mask:0xf bank_mask:0xf bound_ctrl:1
	s_nop 1
	v_max_f32_dpp v42, v43, v43 quad_perm:[2,3,0,1] row_mask:0xf bank_mask:0xf bound_ctrl:1
	s_nop 1
	v_max_f32_dpp v43, v42, v42 row_half_mirror row_mask:0xf bank_mask:0xf bound_ctrl:1
	s_nop 1
	v_max_f32_dpp v42, v43, v43 row_mirror row_mask:0xf bank_mask:0xf bound_ctrl:1
	s_nop 1
	v_mov_b32_e32 v43, v42
	s_nop 1
	v_permlane16_swap_b32_e32 v42, v43
	v_max_f32_e32 v42, v42, v43
	v_mov_b32_e32 v43, v42
	s_nop 1
	v_permlane32_swap_b32_e32 v42, v43
	v_max_f32_e32 v49, v42, v43
	v_mul_f32_e32 v44, 0x3b124925, v49
	s_lshl_b32 s11, s4, 2
	s_add_u32 s11, s11, 0x12a20000
	v_mov_b32_e32 v45, s11
	s_mov_b64 exec, 1
	global_store_dword v45, v44, s[6:7]
	s_mov_b64 exec, -1
	v_mov_b32_e32 v46, 0x43e00000
	v_div_scale_f32 v42, s[100:101], v49, v49, v46
	v_rcp_f32_e32 v43, v42
	s_nop 0
	v_fma_f32 v44, -v42, v43, 1.0
	v_fmac_f32_e32 v43, v44, v43
	v_div_scale_f32 v44, vcc, v46, v49, v46
	v_mul_f32_e32 v45, v44, v43
	v_fma_f32 v47, -v42, v45, v44
	v_fmac_f32_e32 v45, v47, v43
	v_fma_f32 v42, -v42, v45, v44
	s_nop 1
	v_div_fmas_f32 v42, v42, v43, v45
	v_div_fixup_f32 v42, v42, v49, v46
	v_cmp_lt_f32_e32 vcc, 0, v49
	s_nop 1
	v_cndmask_b32_e32 v48, 0, v42, vcc
	v_mul_f32_e32 v76, v76, v48
	v_mul_f32_e32 v77, v77, v48
	v_mul_f32_e32 v78, v78, v48
	v_mul_f32_e32 v79, v79, v48
	v_mul_f32_e32 v80, v80, v48
	v_mul_f32_e32 v81, v81, v48
	v_mul_f32_e32 v82, v82, v48
	v_mul_f32_e32 v83, v83, v48
	v_mul_f32_e32 v84, v84, v48
	v_mul_f32_e32 v85, v85, v48
	v_mul_f32_e32 v86, v86, v48
	v_mul_f32_e32 v87, v87, v48
	v_mul_f32_e32 v88, v88, v48
	v_mul_f32_e32 v89, v89, v48
	v_mul_f32_e32 v90, v90, v48
	v_mul_f32_e32 v91, v91, v48
	v_mul_f32_e32 v92, v92, v48
	v_mul_f32_e32 v93, v93, v48
	v_mul_f32_e32 v94, v94, v48
	v_mul_f32_e32 v95, v95, v48
	v_mul_f32_e32 v96, v96, v48
	v_mul_f32_e32 v97, v97, v48
	v_mul_f32_e32 v98, v98, v48
	v_mul_f32_e32 v99, v99, v48
	v_mul_f32_e32 v100, v100, v48
	v_mul_f32_e32 v101, v101, v48
	v_mul_f32_e32 v102, v102, v48
	v_mul_f32_e32 v103, v103, v48
	v_mul_f32_e32 v104, v104, v48
	v_mul_f32_e32 v105, v105, v48
	v_mul_f32_e32 v106, v106, v48
	v_mul_f32_e32 v107, v107, v48
	v_mov_b32_e32 v58, 0
	v_mov_b32_e32 v59, 0
	v_mov_b32_e32 v60, 0
	v_mov_b32_e32 v61, 0
	v_mov_b32_e32 v62, 0
	v_mov_b32_e32 v63, 0
	v_mov_b32_e32 v64, 0
	v_mov_b32_e32 v65, 0
	v_cvt_pk_fp8_f32 v58, v76, v77
	v_cvt_pk_fp8_f32 v59, v80, v81
	v_cvt_pk_fp8_f32 v60, v84, v85
	v_cvt_pk_fp8_f32 v61, v88, v89
	v_cvt_pk_fp8_f32 v62, v92, v93
	v_cvt_pk_fp8_f32 v63, v96, v97
	v_cvt_pk_fp8_f32 v64, v100, v101
	v_cvt_pk_fp8_f32 v65, v104, v105
	v_cvt_pk_fp8_f32 v58, v78, v79 op_sel:[0,0,1]
	v_cvt_pk_fp8_f32 v59, v82, v83 op_sel:[0,0,1]
	v_cvt_pk_fp8_f32 v60, v86, v87 op_sel:[0,0,1]
	v_cvt_pk_fp8_f32 v61, v90, v91 op_sel:[0,0,1]
	v_cvt_pk_fp8_f32 v62, v94, v95 op_sel:[0,0,1]
	v_cvt_pk_fp8_f32 v63, v98, v99 op_sel:[0,0,1]
	v_cvt_pk_fp8_f32 v64, v102, v103 op_sel:[0,0,1]
	v_cvt_pk_fp8_f32 v65, v106, v107 op_sel:[0,0,1]
	s_and_b32 s11, s4, 0x3fff
	s_lshl_b32 s11, s11, 7
	s_lshr_b32 s101, s4, 14
	s_lshl_b32 s101, s101, 25
	s_add_u32 s11, s11, s101
	v_add_u32_e32 v66, s11, v56
	v_add_u32_e32 v67, 0x400000, v66
	v_add_u32_e32 v68, 0x800000, v66
	v_add_u32_e32 v69, 0xc00000, v66
	v_add_u32_e32 v70, 0x1000000, v66
	v_add_u32_e32 v71, 0x1400000, v66
	v_add_u32_e32 v72, 0x1800000, v66
	v_add_u32_e32 v73, 0x1c00000, v66
	global_store_dword v66, v58, s[6:7]
	global_store_dword v67, v59, s[6:7]
	global_store_dword v68, v60, s[6:7]
	global_store_dword v69, v61, s[6:7]
	global_store_dword v70, v62, s[6:7]
	global_store_dword v71, v63, s[6:7]
	global_store_dword v72, v64, s[6:7]
	global_store_dword v73, v65, s[6:7]
	s_add_u32 s4, s4, s10
	s_cmp_ge_u32 s4, 0x8000
	s_cbranch_scc1 .Ldfv1_done
	s_branch .Ldfv1_loop

.Ldfv1_end:
	v_readlane_b32 s4, v255, 36
	s_waitcnt vmcnt(0)
	s_waitcnt vmcnt(0) lgkmcnt(0)
	s_barrier
	s_mov_b64 s[6:7], exec
	v_readlane_b32 s8, v254, 52
	v_readlane_b32 s9, v254, 53
	s_and_b64 s[8:9], s[6:7], s[8:9]
	s_mov_b64 exec, s[8:9]
	s_cbranch_execz .LBB0_905
	v_readlane_b32 s8, v252, 42
	s_waitcnt vmcnt(0) expcnt(0) lgkmcnt(0)
	s_nop 0
	v_mov_b32_e32 v2, s8
	ds_read_b32 v5, v2
	ds_read_b32 v2, v2 offset:4
	s_waitcnt lgkmcnt(1)
	v_cmp_ne_u32_e32 vcc, 0, v5
	s_cbranch_vccnz .LBB0_873
	v_readlane_b32 s10, v252, 4
	v_readlane_b32 s11, v252, 5
	s_load_dwordx2 s[8:9], s[10:11], 0x4
	s_mov_b32 s15, 1
	s_waitcnt lgkmcnt(0)
	s_mul_i32 s14, s8, s82
	s_mul_i32 s14, s14, s9
	s_branch .LBB0_861
